# o3sc1_1
# speedup vs baseline: 1.0366x; 1.0366x over previous
.LBB0_4:
	s_or_b64 exec, exec, s[2:3]
	v_mov_b32_e32 v1, 0
	s_waitcnt lgkmcnt(0)
	s_barrier
	ds_read2_b32 v[32:33], v1 offset0:3 offset1:7
	ds_read2_b32 v[34:35], v1 offset0:1 offset1:2
	ds_read2_b32 v[36:37], v1 offset0:5 offset1:6
	s_movk_i32 s6, 0xc0
	v_cmp_gt_u32_e32 vcc, s6, v0
	s_movk_i32 s6, 0x80
	s_waitcnt lgkmcnt(2)
	v_fmac_f32_e32 v33, 0, v32
	v_cndmask_b32_e32 v1, 0, v33, vcc
	s_waitcnt lgkmcnt(0)
	v_fma_f32 v32, v35, v1, v37
	v_cmp_gt_u32_e32 vcc, s6, v0
	s_load_dwordx4 s[0:3], s[0:1], 0x30
	s_nop 0
	v_cndmask_b32_e32 v1, v1, v32, vcc
	v_fmac_f32_e32 v36, v34, v1
	v_cmp_gt_u32_e32 vcc, 64, v0
	s_nop 1
	v_cndmask_b32_e32 v0, v1, v36, vcc
	v_mov_b32_e32 v1, s5
	v_fmac_f32_e32 v1, s4, v0
	v_fmac_f32_e32 v24, v28, v1
	v_fmac_f32_e32 v30, v31, v0
	s_nop 0
	v_mov_b32_dpp v1, v24 wave_shl:1 row_mask:0xf bank_mask:0xf
	v_fmac_f32_e32 v13, v23, v1
	v_mov_b32_dpp v0, v30 wave_shl:1 row_mask:0xf bank_mask:0xf
	v_fmac_f32_e32 v12, v22, v13
	v_fmac_f32_e32 v17, v29, v0
	v_fmac_f32_e32 v11, v21, v12
	v_fmac_f32_e32 v16, v27, v17
	v_fmac_f32_e32 v10, v20, v11
	s_waitcnt lgkmcnt(0)
	v_lshl_add_u64 v[20:21], s[0:1], 0, v[18:19]
	v_fmac_f32_e32 v15, v26, v16
	v_pk_add_f32 v[4:5], v[12:13], v[4:5]
	v_pk_add_f32 v[2:3], v[10:11], v[2:3]
	global_store_dwordx4 v[20:21], v[10:13], off sc1 nt
	v_fmac_f32_e32 v14, v25, v15
	v_pk_add_f32 v[0:1], v[14:15], v[6:7]
	v_lshl_add_u64 v[10:11], s[2:3], 0, v[18:19]
	global_store_dwordx4 v[10:11], v[2:5], off sc1 nt
	s_nop 1
	v_pk_add_f32 v[2:3], v[16:17], v[8:9]
	global_store_dwordx4 v[20:21], v[14:17], off offset:1024 sc1 nt
	global_store_dwordx4 v[10:11], v[0:3], off offset:1024 sc1 nt
	s_endpgm
